# NA mask step 2: wave-uniform shortcut for fully masked (wave,tile) pairs (32 v_mov instead of the mask block) and the zero row-offset adds dropped; on top of v13
# speedup vs baseline: 1.0162x; 1.0070x over previous
.LBB0_534:
	v_mad_u64_u32 v[14:15], s[44:45], s42, v241, v[204:205]
	s_mul_i32 s27, s43, 0x3600
	v_add_u32_e32 v15, s27, v15
	s_add_i32 s27, s47, s9
	s_mov_b32 s42, m0
	s_mov_b32 m0, s27
	s_nop 0
	global_load_lds_dwordx4 v[14:15], off
	s_mov_b32 m0, s42
	s_cmp_lt_u32 s26, 4
	s_cbranch_scc1 .LBB0_568
	s_add_i32 s27, s50, s23
	s_add_i32 s27, s27, -5
	s_cmp_gt_u32 s27, 7
	s_cselect_b64 vcc, -1, 0
	s_cbranch_scc1 .Lna_allmask_0
	s_add_i32 s27, s49, s23
	s_add_i32 s27, s27, -5
	s_max_i32 s27, s27, -7
	s_add_i32 s27, s27, 7
	s_min_u32 s27, s27, 14
	s_mulk_i32 s27, 0x7c
	v_add_u32_e32 v161, s27, v228
	v_mov_b32_e32 v15, v223
	ds_read_b32 v160, v161 offset:128
	ds_read_b32 v64, v161
	ds_read_b32 v65, v161 offset:4
	ds_read_b32 v66, v161 offset:8
	ds_read_b32 v67, v161 offset:12
	ds_read_b32 v68, v161 offset:32
	ds_read_b32 v69, v161 offset:36
	v_cmp_gt_u32_e32 vcc, 16, v15
	s_waitcnt lgkmcnt(5)
	v_add_f32_e32 v64, v112, v64
	v_cndmask_b32_e32 v64, v242, v64, vcc
	ds_read_b32 v70, v161 offset:40
	ds_read_b32 v112, v161 offset:132
	v_add_u32_e32 v162, 1, v15
	v_cmp_gt_u32_e32 vcc, 16, v162
	s_waitcnt lgkmcnt(6)
	v_add_f32_e32 v65, v113, v65
	v_cndmask_b32_e32 v65, v242, v65, vcc
	ds_read_b32 v71, v161 offset:44
	ds_read_b32 v113, v161 offset:136
	v_add_u32_e32 v163, 2, v15
	v_cmp_gt_u32_e32 vcc, 16, v163
	s_waitcnt lgkmcnt(7)
	v_add_f32_e32 v66, v114, v66
	v_cndmask_b32_e32 v66, v242, v66, vcc
	ds_read_b32 v72, v161 offset:64
	ds_read_b32 v114, v161 offset:140
	v_add_u32_e32 v164, 3, v15
	v_cmp_gt_u32_e32 vcc, 16, v164
	s_waitcnt lgkmcnt(8)
	v_add_f32_e32 v67, v115, v67
	v_cndmask_b32_e32 v67, v242, v67, vcc
	ds_read_b32 v73, v161 offset:68
	ds_read_b32 v115, v161 offset:160
	v_add_u32_e32 v165, 8, v15
	v_cmp_gt_u32_e32 vcc, 16, v165
	s_waitcnt lgkmcnt(9)
	v_add_f32_e32 v68, v116, v68
	v_cndmask_b32_e32 v68, v242, v68, vcc
	ds_read_b32 v74, v161 offset:72
	ds_read_b32 v116, v161 offset:164
	v_add_u32_e32 v166, 9, v15
	v_cmp_gt_u32_e32 vcc, 16, v166
	s_waitcnt lgkmcnt(10)
	v_add_f32_e32 v69, v117, v69
	v_cndmask_b32_e32 v69, v242, v69, vcc
	ds_read_b32 v75, v161 offset:76
	ds_read_b32 v117, v161 offset:168
	v_add_u32_e32 v167, 10, v15
	v_cmp_gt_u32_e32 vcc, 16, v167
	s_waitcnt lgkmcnt(11)
	v_add_f32_e32 v70, v118, v70
	v_cndmask_b32_e32 v70, v242, v70, vcc
	ds_read_b32 v76, v161 offset:96
	ds_read_b32 v118, v161 offset:172
	v_add_u32_e32 v168, 11, v15
	v_cmp_gt_u32_e32 vcc, 16, v168
	s_waitcnt lgkmcnt(11)
	v_add_f32_e32 v71, v119, v71
	v_cndmask_b32_e32 v71, v242, v71, vcc
	ds_read_b32 v77, v161 offset:100
	ds_read_b32 v119, v161 offset:192
	v_cmp_lt_u32_e32 vcc, s79, v15
	s_waitcnt lgkmcnt(11)
	v_add_f32_e32 v72, v120, v72
	v_cndmask_b32_e32 v72, v242, v72, vcc
	ds_read_b32 v78, v161 offset:104
	ds_read_b32 v120, v161 offset:196
	v_add_u32_e32 v169, 17, v15
	v_cmp_gt_u32_e32 vcc, 16, v169
	s_waitcnt lgkmcnt(11)
	v_add_f32_e32 v73, v121, v73
	v_cndmask_b32_e32 v73, v242, v73, vcc
	ds_read_b32 v79, v161 offset:108
	ds_read_b32 v121, v161 offset:200
	v_add_u32_e32 v170, 18, v15
	v_cmp_gt_u32_e32 vcc, 16, v170
	s_waitcnt lgkmcnt(11)
	v_add_f32_e32 v74, v122, v74
	v_cndmask_b32_e32 v74, v242, v74, vcc
	ds_read_b32 v122, v161 offset:204
	v_add_u32_e32 v171, 19, v15
	v_cmp_gt_u32_e32 vcc, 16, v171
	s_waitcnt lgkmcnt(10)
	v_add_f32_e32 v75, v123, v75
	v_cndmask_b32_e32 v75, v242, v75, vcc
	ds_read_b32 v123, v161 offset:224
	v_add_u32_e32 v172, 24, v15
	v_cmp_gt_u32_e32 vcc, 16, v172
	s_waitcnt lgkmcnt(9)
	v_add_f32_e32 v76, v124, v76
	v_cndmask_b32_e32 v76, v242, v76, vcc
	ds_read_b32 v124, v161 offset:228
	v_add_u32_e32 v173, 25, v15
	v_cmp_gt_u32_e32 vcc, 16, v173
	s_waitcnt lgkmcnt(8)
	v_add_f32_e32 v77, v125, v77
	v_cndmask_b32_e32 v77, v242, v77, vcc
	ds_read_b32 v174, v161 offset:232
	v_add_u32_e32 v175, 26, v15
	v_cmp_gt_u32_e32 vcc, 16, v175
	s_waitcnt lgkmcnt(7)
	v_add_f32_e32 v78, v126, v78
	v_cndmask_b32_e32 v78, v242, v78, vcc
	ds_read_b32 v126, v161 offset:236
	v_add_u32_e32 v125, 27, v15
	v_cmp_gt_u32_e32 vcc, 16, v125
	s_waitcnt lgkmcnt(6)
	v_add_f32_e32 v79, v127, v79
	v_cndmask_b32_e32 v79, v242, v79, vcc
	s_waitcnt lgkmcnt(14)
	v_mov_b32_e32 v127, v160
	v_and_b32_e32 v15, -16, v15
	v_add_f32_e32 v96, v96, v127
	v_cmp_eq_u32_e32 vcc, s76, v15
	v_and_b32_e32 v127, -16, v162
	v_cndmask_b32_e32 v96, v242, v96, vcc
	v_add_f32_e32 v97, v97, v112
	v_cmp_eq_u32_e32 vcc, s76, v127
	s_waitcnt lgkmcnt(13)
	v_mov_b32_e32 v112, v113
	v_and_b32_e32 v113, -16, v163
	v_cndmask_b32_e32 v97, v242, v97, vcc
	v_add_f32_e32 v98, v98, v112
	v_cmp_eq_u32_e32 vcc, s76, v113
	s_waitcnt lgkmcnt(12)
	v_mov_b32_e32 v112, v114
	v_and_b32_e32 v113, -16, v164
	v_cndmask_b32_e32 v98, v242, v98, vcc
	v_add_f32_e32 v99, v99, v112
	v_cmp_eq_u32_e32 vcc, s76, v113
	s_waitcnt lgkmcnt(11)
	v_mov_b32_e32 v112, v115
	v_and_b32_e32 v113, -16, v165
	v_cndmask_b32_e32 v99, v242, v99, vcc
	v_add_f32_e32 v100, v100, v112
	v_cmp_eq_u32_e32 vcc, s76, v113
	s_waitcnt lgkmcnt(10)
	v_mov_b32_e32 v112, v116
	v_and_b32_e32 v113, -16, v166
	v_cndmask_b32_e32 v100, v242, v100, vcc
	v_add_f32_e32 v101, v101, v112
	v_cmp_eq_u32_e32 vcc, s76, v113
	s_waitcnt lgkmcnt(9)
	v_mov_b32_e32 v112, v117
	v_and_b32_e32 v113, -16, v167
	v_cndmask_b32_e32 v101, v242, v101, vcc
	v_add_f32_e32 v102, v102, v112
	v_cmp_eq_u32_e32 vcc, s76, v113
	s_waitcnt lgkmcnt(8)
	v_mov_b32_e32 v112, v118
	v_and_b32_e32 v113, -16, v168
	v_cndmask_b32_e32 v102, v242, v102, vcc
	v_add_f32_e32 v103, v103, v112
	v_cmp_eq_u32_e32 vcc, s76, v113
	s_waitcnt lgkmcnt(7)
	v_mov_b32_e32 v112, v119
	v_add_f32_e32 v104, v104, v112
	v_cndmask_b32_e32 v103, v242, v103, vcc
	v_cmp_eq_u32_e32 vcc, s78, v15
	s_waitcnt lgkmcnt(6)
	v_mov_b32_e32 v15, v120
	v_and_b32_e32 v112, -16, v169
	v_cndmask_b32_e32 v104, v242, v104, vcc
	v_add_f32_e32 v15, v105, v15
	v_cmp_eq_u32_e32 vcc, s76, v112
	v_and_b32_e32 v112, -16, v170
	s_nop 0
	v_cndmask_b32_e32 v105, v242, v15, vcc
	s_waitcnt lgkmcnt(5)
	v_mov_b32_e32 v15, v121
	v_add_f32_e32 v15, v106, v15
	v_cmp_eq_u32_e32 vcc, s76, v112
	v_and_b32_e32 v112, -16, v171
	s_nop 0
	v_cndmask_b32_e32 v106, v242, v15, vcc
	s_waitcnt lgkmcnt(4)
	v_mov_b32_e32 v15, v122
	v_add_f32_e32 v15, v107, v15
	v_cmp_eq_u32_e32 vcc, s76, v112
	v_and_b32_e32 v112, -16, v172
	s_nop 0
	v_cndmask_b32_e32 v107, v242, v15, vcc
	s_waitcnt lgkmcnt(3)
	v_mov_b32_e32 v15, v123
	v_add_f32_e32 v15, v108, v15
	v_cmp_eq_u32_e32 vcc, s76, v112
	v_and_b32_e32 v112, -16, v173
	s_nop 0
	v_cndmask_b32_e32 v108, v242, v15, vcc
	s_waitcnt lgkmcnt(2)
	v_mov_b32_e32 v15, v124
	v_add_f32_e32 v15, v109, v15
	v_cmp_eq_u32_e32 vcc, s76, v112
	v_and_b32_e32 v112, -16, v175
	s_nop 0
	v_cndmask_b32_e32 v109, v242, v15, vcc
	s_waitcnt lgkmcnt(1)
	v_mov_b32_e32 v15, v174
	v_add_f32_e32 v15, v110, v15
	v_cmp_eq_u32_e32 vcc, s76, v112
	s_waitcnt lgkmcnt(0)
	v_mov_b32_e32 v14, v126
	v_add_f32_e32 v14, v111, v14
	v_cndmask_b32_e32 v110, v242, v15, vcc
	v_and_b32_e32 v15, -16, v125
	v_cmp_eq_u32_e32 vcc, s76, v15
	v_mov_b64_e32 v[126:127], v[78:79]
	v_mov_b64_e32 v[124:125], v[76:77]
	v_cndmask_b32_e32 v111, v242, v14, vcc
	v_mov_b64_e32 v[122:123], v[74:75]
	v_mov_b64_e32 v[120:121], v[72:73]
	v_mov_b64_e32 v[118:119], v[70:71]
	v_mov_b64_e32 v[116:117], v[68:69]
	v_mov_b64_e32 v[114:115], v[66:67]
	v_mov_b64_e32 v[112:113], v[64:65]
	s_branch .LBB0_568
.Lna_allmask_0:
	v_mov_b32_e32 v112, v242
	v_mov_b32_e32 v113, v242
	v_mov_b32_e32 v114, v242
	v_mov_b32_e32 v115, v242
	v_mov_b32_e32 v116, v242
	v_mov_b32_e32 v117, v242
	v_mov_b32_e32 v118, v242
	v_mov_b32_e32 v119, v242
	v_mov_b32_e32 v120, v242
	v_mov_b32_e32 v121, v242
	v_mov_b32_e32 v122, v242
	v_mov_b32_e32 v123, v242
	v_mov_b32_e32 v124, v242
	v_mov_b32_e32 v125, v242
	v_mov_b32_e32 v126, v242
	v_mov_b32_e32 v127, v242
	v_mov_b32_e32 v96, v242
	v_mov_b32_e32 v97, v242
	v_mov_b32_e32 v98, v242
	v_mov_b32_e32 v99, v242
	v_mov_b32_e32 v100, v242
	v_mov_b32_e32 v101, v242
	v_mov_b32_e32 v102, v242
	v_mov_b32_e32 v103, v242
	v_mov_b32_e32 v104, v242
	v_mov_b32_e32 v105, v242
	v_mov_b32_e32 v106, v242
	v_mov_b32_e32 v107, v242
	v_mov_b32_e32 v108, v242
	v_mov_b32_e32 v109, v242
	v_mov_b32_e32 v110, v242
	v_mov_b32_e32 v111, v242

.LBB0_573:
	s_add_i32 s27, s47, 0x2000
	s_cmpk_lg_i32 s47, 0x4000
	s_cselect_b32 s64, s27, 0
	v_mad_u64_u32 v[96:97], s[44:45], s42, v241, v[204:205]
	s_mul_i32 s27, s43, 0x3600
	v_add_u32_e32 v97, s27, v97
	s_add_i32 s27, s64, s9
	s_cmp_lt_u32 s26, 3
	s_mov_b32 s26, m0
	s_mov_b32 m0, s27
	s_nop 0
	global_load_lds_dwordx4 v[96:97], off
	s_mov_b32 m0, s26
	s_cbranch_scc1 .LBB0_607
	s_add_i32 s26, s50, s23
	s_add_i32 s26, s26, -4
	s_cmp_gt_u32 s26, 7
	s_cselect_b64 vcc, -1, 0
	s_cbranch_scc1 .Lna_allmask_1
	s_add_i32 s26, s49, s23
	s_add_i32 s26, s26, -4
	s_max_i32 s26, s26, -7
	s_add_i32 s26, s26, 7
	s_min_u32 s26, s26, 14
	s_mulk_i32 s26, 0x7c
	v_add_u32_e32 v166, s26, v228
	v_mov_b32_e32 v164, v223
	ds_read_b32 v165, v166 offset:128
	ds_read_b32 v96, v166
	ds_read_b32 v97, v166 offset:4
	ds_read_b32 v98, v166 offset:8
	ds_read_b32 v99, v166 offset:12
	ds_read_b32 v100, v166 offset:32
	ds_read_b32 v101, v166 offset:36
	v_cmp_gt_u32_e32 vcc, 16, v164
	s_waitcnt lgkmcnt(5)
	v_add_f32_e32 v96, v80, v96
	v_cndmask_b32_e32 v96, v242, v96, vcc
	ds_read_b32 v102, v166 offset:40
	ds_read_b32 v80, v166 offset:132
	v_add_u32_e32 v167, 1, v164
	v_cmp_gt_u32_e32 vcc, 16, v167
	s_waitcnt lgkmcnt(6)
	v_add_f32_e32 v97, v81, v97
	v_cndmask_b32_e32 v97, v242, v97, vcc
	ds_read_b32 v103, v166 offset:44
	ds_read_b32 v81, v166 offset:136
	v_add_u32_e32 v168, 2, v164
	v_cmp_gt_u32_e32 vcc, 16, v168
	s_waitcnt lgkmcnt(7)
	v_add_f32_e32 v98, v82, v98
	v_cndmask_b32_e32 v98, v242, v98, vcc
	ds_read_b32 v104, v166 offset:64
	ds_read_b32 v82, v166 offset:140
	v_add_u32_e32 v169, 3, v164
	v_cmp_gt_u32_e32 vcc, 16, v169
	s_waitcnt lgkmcnt(8)
	v_add_f32_e32 v99, v83, v99
	v_cndmask_b32_e32 v99, v242, v99, vcc
	ds_read_b32 v105, v166 offset:68
	ds_read_b32 v83, v166 offset:160
	v_add_u32_e32 v170, 8, v164
	v_cmp_gt_u32_e32 vcc, 16, v170
	s_waitcnt lgkmcnt(9)
	v_add_f32_e32 v100, v84, v100
	v_cndmask_b32_e32 v100, v242, v100, vcc
	ds_read_b32 v106, v166 offset:72
	ds_read_b32 v84, v166 offset:164
	v_add_u32_e32 v171, 9, v164
	v_cmp_gt_u32_e32 vcc, 16, v171
	s_waitcnt lgkmcnt(10)
	v_add_f32_e32 v101, v85, v101
	v_cndmask_b32_e32 v101, v242, v101, vcc
	ds_read_b32 v107, v166 offset:76
	ds_read_b32 v85, v166 offset:168
	v_add_u32_e32 v172, 10, v164
	v_cmp_gt_u32_e32 vcc, 16, v172
	s_waitcnt lgkmcnt(11)
	v_add_f32_e32 v102, v86, v102
	v_cndmask_b32_e32 v102, v242, v102, vcc
	ds_read_b32 v108, v166 offset:96
	ds_read_b32 v86, v166 offset:172
	v_add_u32_e32 v173, 11, v164
	v_cmp_gt_u32_e32 vcc, 16, v173
	s_waitcnt lgkmcnt(11)
	v_add_f32_e32 v103, v87, v103
	v_cndmask_b32_e32 v103, v242, v103, vcc
	ds_read_b32 v109, v166 offset:100
	ds_read_b32 v87, v166 offset:192
	v_cmp_lt_u32_e32 vcc, s79, v164
	s_waitcnt lgkmcnt(11)
	v_add_f32_e32 v104, v88, v104
	v_cndmask_b32_e32 v104, v242, v104, vcc
	ds_read_b32 v110, v166 offset:104
	ds_read_b32 v88, v166 offset:196
	v_add_u32_e32 v174, 17, v164
	v_cmp_gt_u32_e32 vcc, 16, v174
	s_waitcnt lgkmcnt(11)
	v_add_f32_e32 v105, v89, v105
	v_cndmask_b32_e32 v105, v242, v105, vcc
	ds_read_b32 v111, v166 offset:108
	ds_read_b32 v89, v166 offset:200
	v_add_u32_e32 v175, 18, v164
	v_cmp_gt_u32_e32 vcc, 16, v175
	s_waitcnt lgkmcnt(11)
	v_add_f32_e32 v106, v90, v106
	v_cndmask_b32_e32 v106, v242, v106, vcc
	ds_read_b32 v90, v166 offset:204
	v_add_u32_e32 v176, 19, v164
	v_cmp_gt_u32_e32 vcc, 16, v176
	s_waitcnt lgkmcnt(10)
	v_add_f32_e32 v107, v91, v107
	v_cndmask_b32_e32 v107, v242, v107, vcc
	ds_read_b32 v91, v166 offset:224
	v_add_u32_e32 v177, 24, v164
	v_cmp_gt_u32_e32 vcc, 16, v177
	s_waitcnt lgkmcnt(9)
	v_add_f32_e32 v108, v92, v108
	v_cndmask_b32_e32 v108, v242, v108, vcc
	ds_read_b32 v92, v166 offset:228
	v_add_u32_e32 v178, 25, v164
	v_cmp_gt_u32_e32 vcc, 16, v178
	s_waitcnt lgkmcnt(8)
	v_add_f32_e32 v109, v93, v109
	v_cndmask_b32_e32 v109, v242, v109, vcc
	ds_read_b32 v179, v166 offset:232
	v_add_u32_e32 v180, 26, v164
	v_cmp_gt_u32_e32 vcc, 16, v180
	s_waitcnt lgkmcnt(7)
	v_add_f32_e32 v110, v94, v110
	v_cndmask_b32_e32 v110, v242, v110, vcc
	ds_read_b32 v94, v166 offset:236
	v_add_u32_e32 v93, 27, v164
	v_cmp_gt_u32_e32 vcc, 16, v93
	s_waitcnt lgkmcnt(6)
	v_add_f32_e32 v111, v95, v111
	v_cndmask_b32_e32 v111, v242, v111, vcc
	s_waitcnt lgkmcnt(14)
	v_mov_b32_e32 v95, v165
	v_and_b32_e32 v164, -16, v164
	v_add_f32_e32 v64, v64, v95
	v_cmp_eq_u32_e32 vcc, s76, v164
	v_and_b32_e32 v95, -16, v167
	v_cndmask_b32_e32 v64, v242, v64, vcc
	v_add_f32_e32 v65, v65, v80
	v_cmp_eq_u32_e32 vcc, s76, v95
	s_waitcnt lgkmcnt(13)
	v_mov_b32_e32 v80, v81
	v_and_b32_e32 v81, -16, v168
	v_cndmask_b32_e32 v65, v242, v65, vcc
	v_add_f32_e32 v66, v66, v80
	v_cmp_eq_u32_e32 vcc, s76, v81
	s_waitcnt lgkmcnt(12)
	v_mov_b32_e32 v80, v82
	v_and_b32_e32 v81, -16, v169
	v_cndmask_b32_e32 v66, v242, v66, vcc
	v_add_f32_e32 v67, v67, v80
	v_cmp_eq_u32_e32 vcc, s76, v81
	s_waitcnt lgkmcnt(11)
	v_mov_b32_e32 v80, v83
	v_and_b32_e32 v81, -16, v170
	v_cndmask_b32_e32 v67, v242, v67, vcc
	v_add_f32_e32 v68, v68, v80
	v_cmp_eq_u32_e32 vcc, s76, v81
	s_waitcnt lgkmcnt(10)
	v_mov_b32_e32 v80, v84
	v_and_b32_e32 v81, -16, v171
	v_cndmask_b32_e32 v68, v242, v68, vcc
	v_add_f32_e32 v69, v69, v80
	v_cmp_eq_u32_e32 vcc, s76, v81
	s_waitcnt lgkmcnt(9)
	v_mov_b32_e32 v80, v85
	v_and_b32_e32 v81, -16, v172
	v_cndmask_b32_e32 v69, v242, v69, vcc
	v_add_f32_e32 v70, v70, v80
	v_cmp_eq_u32_e32 vcc, s76, v81
	s_waitcnt lgkmcnt(8)
	v_mov_b32_e32 v80, v86
	v_and_b32_e32 v81, -16, v173
	v_cndmask_b32_e32 v70, v242, v70, vcc
	v_add_f32_e32 v71, v71, v80
	v_cmp_eq_u32_e32 vcc, s76, v81
	s_waitcnt lgkmcnt(7)
	v_mov_b32_e32 v80, v87
	v_add_f32_e32 v72, v72, v80
	v_cndmask_b32_e32 v71, v242, v71, vcc
	v_cmp_eq_u32_e32 vcc, s78, v164
	s_waitcnt lgkmcnt(6)
	v_mov_b32_e32 v80, v88
	v_and_b32_e32 v81, -16, v174
	v_cndmask_b32_e32 v72, v242, v72, vcc
	v_add_f32_e32 v73, v73, v80
	v_cmp_eq_u32_e32 vcc, s76, v81
	s_waitcnt lgkmcnt(5)
	v_mov_b32_e32 v80, v89
	v_and_b32_e32 v81, -16, v175
	v_cndmask_b32_e32 v73, v242, v73, vcc
	v_add_f32_e32 v74, v74, v80
	v_cmp_eq_u32_e32 vcc, s76, v81
	s_waitcnt lgkmcnt(4)
	v_mov_b32_e32 v80, v90
	v_and_b32_e32 v81, -16, v176
	v_cndmask_b32_e32 v74, v242, v74, vcc
	v_add_f32_e32 v75, v75, v80
	v_cmp_eq_u32_e32 vcc, s76, v81
	s_waitcnt lgkmcnt(3)
	v_mov_b32_e32 v80, v91
	v_and_b32_e32 v81, -16, v177
	v_cndmask_b32_e32 v75, v242, v75, vcc
	v_add_f32_e32 v76, v76, v80
	v_cmp_eq_u32_e32 vcc, s76, v81
	s_waitcnt lgkmcnt(2)
	v_mov_b32_e32 v80, v92
	v_and_b32_e32 v81, -16, v178
	v_cndmask_b32_e32 v76, v242, v76, vcc
	v_add_f32_e32 v77, v77, v80
	v_cmp_eq_u32_e32 vcc, s76, v81
	s_waitcnt lgkmcnt(1)
	v_mov_b32_e32 v80, v179
	v_and_b32_e32 v81, -16, v180
	v_cndmask_b32_e32 v77, v242, v77, vcc
	v_add_f32_e32 v78, v78, v80
	v_cmp_eq_u32_e32 vcc, s76, v81
	s_waitcnt lgkmcnt(0)
	v_mov_b32_e32 v15, v94
	v_and_b32_e32 v80, -16, v93
	v_cndmask_b32_e32 v78, v242, v78, vcc
	v_add_f32_e32 v15, v79, v15
	v_cmp_eq_u32_e32 vcc, s76, v80
	v_mov_b64_e32 v[80:81], v[96:97]
	v_mov_b64_e32 v[82:83], v[98:99]
	v_cndmask_b32_e32 v79, v242, v15, vcc
	v_mov_b64_e32 v[84:85], v[100:101]
	v_mov_b64_e32 v[86:87], v[102:103]
	v_mov_b64_e32 v[88:89], v[104:105]
	v_mov_b64_e32 v[90:91], v[106:107]
	v_mov_b64_e32 v[92:93], v[108:109]
	v_mov_b64_e32 v[94:95], v[110:111]
	s_branch .LBB0_607
.Lna_allmask_1:
	v_mov_b32_e32 v80, v242
	v_mov_b32_e32 v81, v242
	v_mov_b32_e32 v82, v242
	v_mov_b32_e32 v83, v242
	v_mov_b32_e32 v84, v242
	v_mov_b32_e32 v85, v242
	v_mov_b32_e32 v86, v242
	v_mov_b32_e32 v87, v242
	v_mov_b32_e32 v88, v242
	v_mov_b32_e32 v89, v242
	v_mov_b32_e32 v90, v242
	v_mov_b32_e32 v91, v242
	v_mov_b32_e32 v92, v242
	v_mov_b32_e32 v93, v242
	v_mov_b32_e32 v94, v242
	v_mov_b32_e32 v95, v242
	v_mov_b32_e32 v64, v242
	v_mov_b32_e32 v65, v242
	v_mov_b32_e32 v66, v242
	v_mov_b32_e32 v67, v242
	v_mov_b32_e32 v68, v242
	v_mov_b32_e32 v69, v242
	v_mov_b32_e32 v70, v242
	v_mov_b32_e32 v71, v242
	v_mov_b32_e32 v72, v242
	v_mov_b32_e32 v73, v242
	v_mov_b32_e32 v74, v242
	v_mov_b32_e32 v75, v242
	v_mov_b32_e32 v76, v242
	v_mov_b32_e32 v77, v242
	v_mov_b32_e32 v78, v242
	v_mov_b32_e32 v79, v242

.LBB0_625:
	v_mad_u64_u32 v[64:65], s[46:47], s6, v241, v[204:205]
	s_mul_i32 s6, s7, 0x3600
	v_add_u32_e32 v65, s6, v65
	s_add_i32 s6, s81, s9
	s_mov_b32 s7, m0
	s_mov_b32 m0, s6
	s_nop 0
	global_load_lds_dwordx4 v[64:65], off
	s_mov_b32 m0, s7
	s_cmp_lt_u32 s50, 4
	s_cbranch_scc1 .LBB0_659
	s_add_i32 s6, s23, s90
	s_add_i32 s6, s6, -8
	s_cmp_gt_u32 s6, 7
	s_cselect_b64 vcc, -1, 0
	s_cbranch_scc1 .Lna_allmask_2
	s_add_i32 s6, s23, s74
	s_max_i32 s6, s6, -7
	s_add_i32 s6, s6, 7
	s_min_u32 s6, s6, 14
	s_mulk_i32 s6, 0x7c
	v_add_u32_e32 v163, s6, v228
	v_mov_b32_e32 v161, v223
	ds_read_b32 v162, v163 offset:128
	ds_read_b32 v64, v163
	ds_read_b32 v65, v163 offset:4
	ds_read_b32 v66, v163 offset:8
	ds_read_b32 v67, v163 offset:12
	ds_read_b32 v68, v163 offset:32
	ds_read_b32 v69, v163 offset:36
	v_cmp_gt_u32_e32 vcc, 16, v161
	s_waitcnt lgkmcnt(5)
	v_add_f32_e32 v64, v112, v64
	v_cndmask_b32_e32 v64, v242, v64, vcc
	ds_read_b32 v70, v163 offset:40
	ds_read_b32 v112, v163 offset:132
	v_add_u32_e32 v164, 1, v161
	v_cmp_gt_u32_e32 vcc, 16, v164
	s_waitcnt lgkmcnt(6)
	v_add_f32_e32 v65, v113, v65
	v_cndmask_b32_e32 v65, v242, v65, vcc
	ds_read_b32 v71, v163 offset:44
	ds_read_b32 v113, v163 offset:136
	v_add_u32_e32 v165, 2, v161
	v_cmp_gt_u32_e32 vcc, 16, v165
	s_waitcnt lgkmcnt(7)
	v_add_f32_e32 v66, v114, v66
	v_cndmask_b32_e32 v66, v242, v66, vcc
	ds_read_b32 v72, v163 offset:64
	ds_read_b32 v114, v163 offset:140
	v_add_u32_e32 v166, 3, v161
	v_cmp_gt_u32_e32 vcc, 16, v166
	s_waitcnt lgkmcnt(8)
	v_add_f32_e32 v67, v115, v67
	v_cndmask_b32_e32 v67, v242, v67, vcc
	ds_read_b32 v73, v163 offset:68
	ds_read_b32 v115, v163 offset:160
	v_add_u32_e32 v167, 8, v161
	v_cmp_gt_u32_e32 vcc, 16, v167
	s_waitcnt lgkmcnt(9)
	v_add_f32_e32 v68, v116, v68
	v_cndmask_b32_e32 v68, v242, v68, vcc
	ds_read_b32 v74, v163 offset:72
	ds_read_b32 v116, v163 offset:164
	v_add_u32_e32 v168, 9, v161
	v_cmp_gt_u32_e32 vcc, 16, v168
	s_waitcnt lgkmcnt(10)
	v_add_f32_e32 v69, v117, v69
	v_cndmask_b32_e32 v69, v242, v69, vcc
	ds_read_b32 v75, v163 offset:76
	ds_read_b32 v117, v163 offset:168
	v_add_u32_e32 v169, 10, v161
	v_cmp_gt_u32_e32 vcc, 16, v169
	s_waitcnt lgkmcnt(11)
	v_add_f32_e32 v70, v118, v70
	v_cndmask_b32_e32 v70, v242, v70, vcc
	ds_read_b32 v76, v163 offset:96
	ds_read_b32 v118, v163 offset:172
	v_add_u32_e32 v170, 11, v161
	v_cmp_gt_u32_e32 vcc, 16, v170
	s_waitcnt lgkmcnt(11)
	v_add_f32_e32 v71, v119, v71
	v_cndmask_b32_e32 v71, v242, v71, vcc
	ds_read_b32 v77, v163 offset:100
	ds_read_b32 v119, v163 offset:192
	v_cmp_lt_u32_e32 vcc, s79, v161
	s_waitcnt lgkmcnt(11)
	v_add_f32_e32 v72, v120, v72
	v_cndmask_b32_e32 v72, v242, v72, vcc
	ds_read_b32 v78, v163 offset:104
	ds_read_b32 v120, v163 offset:196
	v_add_u32_e32 v171, 17, v161
	v_cmp_gt_u32_e32 vcc, 16, v171
	s_waitcnt lgkmcnt(11)
	v_add_f32_e32 v73, v121, v73
	v_cndmask_b32_e32 v73, v242, v73, vcc
	ds_read_b32 v79, v163 offset:108
	ds_read_b32 v121, v163 offset:200
	v_add_u32_e32 v172, 18, v161
	v_cmp_gt_u32_e32 vcc, 16, v172
	s_waitcnt lgkmcnt(11)
	v_add_f32_e32 v74, v122, v74
	v_cndmask_b32_e32 v74, v242, v74, vcc
	ds_read_b32 v122, v163 offset:204
	v_add_u32_e32 v173, 19, v161
	v_cmp_gt_u32_e32 vcc, 16, v173
	s_waitcnt lgkmcnt(10)
	v_add_f32_e32 v75, v123, v75
	v_cndmask_b32_e32 v75, v242, v75, vcc
	ds_read_b32 v123, v163 offset:224
	v_add_u32_e32 v174, 24, v161
	v_cmp_gt_u32_e32 vcc, 16, v174
	s_waitcnt lgkmcnt(9)
	v_add_f32_e32 v76, v124, v76
	v_cndmask_b32_e32 v76, v242, v76, vcc
	ds_read_b32 v124, v163 offset:228
	v_add_u32_e32 v175, 25, v161
	v_cmp_gt_u32_e32 vcc, 16, v175
	s_waitcnt lgkmcnt(8)
	v_add_f32_e32 v77, v125, v77
	v_cndmask_b32_e32 v77, v242, v77, vcc
	ds_read_b32 v176, v163 offset:232
	v_add_u32_e32 v177, 26, v161
	v_cmp_gt_u32_e32 vcc, 16, v177
	s_waitcnt lgkmcnt(7)
	v_add_f32_e32 v78, v126, v78
	v_cndmask_b32_e32 v78, v242, v78, vcc
	ds_read_b32 v126, v163 offset:236
	v_add_u32_e32 v125, 27, v161
	v_cmp_gt_u32_e32 vcc, 16, v125
	s_waitcnt lgkmcnt(6)
	v_add_f32_e32 v79, v127, v79
	v_cndmask_b32_e32 v79, v242, v79, vcc
	s_waitcnt lgkmcnt(14)
	v_mov_b32_e32 v127, v162
	v_and_b32_e32 v161, -16, v161
	v_add_f32_e32 v96, v96, v127
	v_cmp_eq_u32_e32 vcc, s76, v161
	v_and_b32_e32 v127, -16, v164
	v_cndmask_b32_e32 v96, v242, v96, vcc
	v_add_f32_e32 v97, v97, v112
	v_cmp_eq_u32_e32 vcc, s76, v127
	s_waitcnt lgkmcnt(13)
	v_mov_b32_e32 v112, v113
	v_and_b32_e32 v113, -16, v165
	v_cndmask_b32_e32 v97, v242, v97, vcc
	v_add_f32_e32 v98, v98, v112
	v_cmp_eq_u32_e32 vcc, s76, v113
	s_waitcnt lgkmcnt(12)
	v_mov_b32_e32 v112, v114
	v_and_b32_e32 v113, -16, v166
	v_cndmask_b32_e32 v98, v242, v98, vcc
	v_add_f32_e32 v99, v99, v112
	v_cmp_eq_u32_e32 vcc, s76, v113
	s_waitcnt lgkmcnt(11)
	v_mov_b32_e32 v112, v115
	v_and_b32_e32 v113, -16, v167
	v_cndmask_b32_e32 v99, v242, v99, vcc
	v_add_f32_e32 v100, v100, v112
	v_cmp_eq_u32_e32 vcc, s76, v113
	s_waitcnt lgkmcnt(10)
	v_mov_b32_e32 v112, v116
	v_and_b32_e32 v113, -16, v168
	v_cndmask_b32_e32 v100, v242, v100, vcc
	v_add_f32_e32 v101, v101, v112
	v_cmp_eq_u32_e32 vcc, s76, v113
	s_waitcnt lgkmcnt(9)
	v_mov_b32_e32 v112, v117
	v_and_b32_e32 v113, -16, v169
	v_cndmask_b32_e32 v101, v242, v101, vcc
	v_add_f32_e32 v102, v102, v112
	v_cmp_eq_u32_e32 vcc, s76, v113
	s_waitcnt lgkmcnt(8)
	v_mov_b32_e32 v112, v118
	v_and_b32_e32 v113, -16, v170
	v_cndmask_b32_e32 v102, v242, v102, vcc
	v_add_f32_e32 v103, v103, v112
	v_cmp_eq_u32_e32 vcc, s76, v113
	s_waitcnt lgkmcnt(7)
	v_mov_b32_e32 v112, v119
	v_add_f32_e32 v104, v104, v112
	v_cndmask_b32_e32 v103, v242, v103, vcc
	v_cmp_eq_u32_e32 vcc, s78, v161
	s_waitcnt lgkmcnt(6)
	v_mov_b32_e32 v112, v120
	v_and_b32_e32 v113, -16, v171
	v_cndmask_b32_e32 v104, v242, v104, vcc
	v_add_f32_e32 v105, v105, v112
	v_cmp_eq_u32_e32 vcc, s76, v113
	s_waitcnt lgkmcnt(5)
	v_mov_b32_e32 v112, v121
	v_and_b32_e32 v113, -16, v172
	v_cndmask_b32_e32 v105, v242, v105, vcc
	v_add_f32_e32 v106, v106, v112
	v_cmp_eq_u32_e32 vcc, s76, v113
	s_waitcnt lgkmcnt(4)
	v_mov_b32_e32 v112, v122
	v_and_b32_e32 v113, -16, v173
	v_cndmask_b32_e32 v106, v242, v106, vcc
	v_add_f32_e32 v107, v107, v112
	v_cmp_eq_u32_e32 vcc, s76, v113
	s_waitcnt lgkmcnt(3)
	v_mov_b32_e32 v112, v123
	v_and_b32_e32 v113, -16, v174
	v_cndmask_b32_e32 v107, v242, v107, vcc
	v_add_f32_e32 v108, v108, v112
	v_cmp_eq_u32_e32 vcc, s76, v113
	s_waitcnt lgkmcnt(2)
	v_mov_b32_e32 v112, v124
	v_and_b32_e32 v113, -16, v175
	v_cndmask_b32_e32 v108, v242, v108, vcc
	v_add_f32_e32 v109, v109, v112
	v_cmp_eq_u32_e32 vcc, s76, v113
	s_waitcnt lgkmcnt(1)
	v_mov_b32_e32 v112, v176
	v_and_b32_e32 v113, -16, v177
	v_cndmask_b32_e32 v109, v242, v109, vcc
	v_add_f32_e32 v110, v110, v112
	v_cmp_eq_u32_e32 vcc, s76, v113
	s_waitcnt lgkmcnt(0)
	v_mov_b32_e32 v112, v126
	v_and_b32_e32 v113, -16, v125
	v_cndmask_b32_e32 v110, v242, v110, vcc
	v_add_f32_e32 v111, v111, v112
	v_cmp_eq_u32_e32 vcc, s76, v113
	v_mov_b64_e32 v[126:127], v[78:79]
	v_mov_b64_e32 v[124:125], v[76:77]
	v_cndmask_b32_e32 v111, v242, v111, vcc
	v_mov_b64_e32 v[122:123], v[74:75]
	v_mov_b64_e32 v[120:121], v[72:73]
	v_mov_b64_e32 v[118:119], v[70:71]
	v_mov_b64_e32 v[116:117], v[68:69]
	v_mov_b64_e32 v[114:115], v[66:67]
	v_mov_b64_e32 v[112:113], v[64:65]
	s_branch .LBB0_659

.LBB0_672:
	s_cmp_lt_u32 s50, 3
	s_cbranch_scc1 .LBB0_706
	s_add_i32 s6, s23, s90
	s_add_i32 s6, s6, -7
	s_cmp_gt_u32 s6, 7
	s_cselect_b64 vcc, -1, 0
	s_cbranch_scc1 .Lna_allmask_3
	s_add_i32 s6, s23, s27
	s_max_i32 s6, s6, -7
	s_add_i32 s6, s6, 7
	s_min_u32 s6, s6, 14
	s_mulk_i32 s6, 0x7c
	v_add_u32_e32 v124, s6, v228
	v_mov_b32_e32 v122, v223
	ds_read_b32 v123, v124 offset:128
	ds_read_b32 v96, v124
	ds_read_b32 v97, v124 offset:4
	ds_read_b32 v98, v124 offset:8
	ds_read_b32 v99, v124 offset:12
	ds_read_b32 v100, v124 offset:32
	ds_read_b32 v101, v124 offset:36
	v_cmp_gt_u32_e32 vcc, 16, v122
	s_waitcnt lgkmcnt(5)
	v_add_f32_e32 v96, v80, v96
	v_cndmask_b32_e32 v96, v242, v96, vcc
	ds_read_b32 v102, v124 offset:40
	ds_read_b32 v80, v124 offset:132
	v_add_u32_e32 v125, 1, v122
	v_cmp_gt_u32_e32 vcc, 16, v125
	s_waitcnt lgkmcnt(6)
	v_add_f32_e32 v97, v81, v97
	v_cndmask_b32_e32 v97, v242, v97, vcc
	ds_read_b32 v103, v124 offset:44
	ds_read_b32 v81, v124 offset:136
	v_add_u32_e32 v126, 2, v122
	v_cmp_gt_u32_e32 vcc, 16, v126
	s_waitcnt lgkmcnt(7)
	v_add_f32_e32 v98, v82, v98
	v_cndmask_b32_e32 v98, v242, v98, vcc
	ds_read_b32 v104, v124 offset:64
	ds_read_b32 v82, v124 offset:140
	v_add_u32_e32 v127, 3, v122
	v_cmp_gt_u32_e32 vcc, 16, v127
	s_waitcnt lgkmcnt(8)
	v_add_f32_e32 v99, v83, v99
	v_cndmask_b32_e32 v99, v242, v99, vcc
	ds_read_b32 v105, v124 offset:68
	ds_read_b32 v83, v124 offset:160
	v_add_u32_e32 v229, 8, v122
	v_cmp_gt_u32_e32 vcc, 16, v229
	s_waitcnt lgkmcnt(9)
	v_add_f32_e32 v100, v84, v100
	v_cndmask_b32_e32 v100, v242, v100, vcc
	ds_read_b32 v106, v124 offset:72
	ds_read_b32 v84, v124 offset:164
	v_add_u32_e32 v230, 9, v122
	v_cmp_gt_u32_e32 vcc, 16, v230
	s_waitcnt lgkmcnt(10)
	v_add_f32_e32 v101, v85, v101
	v_cndmask_b32_e32 v101, v242, v101, vcc
	ds_read_b32 v107, v124 offset:76
	ds_read_b32 v85, v124 offset:168
	v_add_u32_e32 v231, 10, v122
	v_cmp_gt_u32_e32 vcc, 16, v231
	s_waitcnt lgkmcnt(11)
	v_add_f32_e32 v102, v86, v102
	v_cndmask_b32_e32 v102, v242, v102, vcc
	ds_read_b32 v108, v124 offset:96
	ds_read_b32 v86, v124 offset:172
	v_add_u32_e32 v232, 11, v122
	v_cmp_gt_u32_e32 vcc, 16, v232
	s_waitcnt lgkmcnt(11)
	v_add_f32_e32 v103, v87, v103
	v_cndmask_b32_e32 v103, v242, v103, vcc
	ds_read_b32 v109, v124 offset:100
	ds_read_b32 v87, v124 offset:192
	v_cmp_lt_u32_e32 vcc, s79, v122
	s_waitcnt lgkmcnt(11)
	v_add_f32_e32 v104, v88, v104
	v_cndmask_b32_e32 v104, v242, v104, vcc
	ds_read_b32 v110, v124 offset:104
	ds_read_b32 v88, v124 offset:196
	v_add_u32_e32 v233, 17, v122
	v_cmp_gt_u32_e32 vcc, 16, v233
	s_waitcnt lgkmcnt(11)
	v_add_f32_e32 v105, v89, v105
	v_cndmask_b32_e32 v105, v242, v105, vcc
	ds_read_b32 v111, v124 offset:108
	ds_read_b32 v89, v124 offset:200
	v_add_u32_e32 v247, 18, v122
	v_cmp_gt_u32_e32 vcc, 16, v247
	s_waitcnt lgkmcnt(11)
	v_add_f32_e32 v106, v90, v106
	v_cndmask_b32_e32 v106, v242, v106, vcc
	ds_read_b32 v90, v124 offset:204
	v_add_u32_e32 v248, 19, v122
	v_cmp_gt_u32_e32 vcc, 16, v248
	s_waitcnt lgkmcnt(10)
	v_add_f32_e32 v107, v91, v107
	v_cndmask_b32_e32 v107, v242, v107, vcc
	ds_read_b32 v91, v124 offset:224
	v_add_u32_e32 v249, 24, v122
	v_cmp_gt_u32_e32 vcc, 16, v249
	s_waitcnt lgkmcnt(9)
	v_add_f32_e32 v108, v92, v108
	v_cndmask_b32_e32 v108, v242, v108, vcc
	ds_read_b32 v92, v124 offset:228
	v_add_u32_e32 v250, 25, v122
	v_cmp_gt_u32_e32 vcc, 16, v250
	s_waitcnt lgkmcnt(8)
	v_add_f32_e32 v109, v93, v109
	v_cndmask_b32_e32 v109, v242, v109, vcc
	ds_read_b32 v251, v124 offset:232
	v_add_u32_e32 v239, 26, v122
	v_cmp_gt_u32_e32 vcc, 16, v239
	s_waitcnt lgkmcnt(7)
	v_add_f32_e32 v110, v94, v110
	v_cndmask_b32_e32 v110, v242, v110, vcc
	ds_read_b32 v94, v124 offset:236
	v_add_u32_e32 v93, 27, v122
	v_cmp_gt_u32_e32 vcc, 16, v93
	s_waitcnt lgkmcnt(6)
	v_add_f32_e32 v111, v95, v111
	v_cndmask_b32_e32 v111, v242, v111, vcc
	s_waitcnt lgkmcnt(14)
	v_mov_b32_e32 v95, v123
	v_and_b32_e32 v122, -16, v122
	v_add_f32_e32 v64, v64, v95
	v_cmp_eq_u32_e32 vcc, s76, v122
	v_and_b32_e32 v95, -16, v125
	v_cndmask_b32_e32 v64, v242, v64, vcc
	v_add_f32_e32 v65, v65, v80
	v_cmp_eq_u32_e32 vcc, s76, v95
	s_waitcnt lgkmcnt(13)
	v_mov_b32_e32 v80, v81
	v_and_b32_e32 v81, -16, v126
	v_cndmask_b32_e32 v65, v242, v65, vcc
	v_add_f32_e32 v66, v66, v80
	v_cmp_eq_u32_e32 vcc, s76, v81
	s_waitcnt lgkmcnt(12)
	v_mov_b32_e32 v80, v82
	v_and_b32_e32 v81, -16, v127
	v_cndmask_b32_e32 v66, v242, v66, vcc
	v_add_f32_e32 v67, v67, v80
	v_cmp_eq_u32_e32 vcc, s76, v81
	s_waitcnt lgkmcnt(11)
	v_mov_b32_e32 v80, v83
	v_and_b32_e32 v81, -16, v229
	v_cndmask_b32_e32 v67, v242, v67, vcc
	v_add_f32_e32 v68, v68, v80
	v_cmp_eq_u32_e32 vcc, s76, v81
	s_waitcnt lgkmcnt(10)
	v_mov_b32_e32 v80, v84
	v_and_b32_e32 v81, -16, v230
	v_cndmask_b32_e32 v68, v242, v68, vcc
	v_add_f32_e32 v69, v69, v80
	v_cmp_eq_u32_e32 vcc, s76, v81
	s_waitcnt lgkmcnt(9)
	v_mov_b32_e32 v80, v85
	v_and_b32_e32 v81, -16, v231
	v_cndmask_b32_e32 v69, v242, v69, vcc
	v_add_f32_e32 v70, v70, v80
	v_cmp_eq_u32_e32 vcc, s76, v81
	s_waitcnt lgkmcnt(8)
	v_mov_b32_e32 v80, v86
	v_and_b32_e32 v81, -16, v232
	v_cndmask_b32_e32 v70, v242, v70, vcc
	v_add_f32_e32 v71, v71, v80
	v_cmp_eq_u32_e32 vcc, s76, v81
	s_waitcnt lgkmcnt(7)
	v_mov_b32_e32 v80, v87
	v_add_f32_e32 v72, v72, v80
	v_cndmask_b32_e32 v71, v242, v71, vcc
	v_cmp_eq_u32_e32 vcc, s78, v122
	s_waitcnt lgkmcnt(6)
	v_mov_b32_e32 v80, v88
	v_and_b32_e32 v81, -16, v233
	v_cndmask_b32_e32 v72, v242, v72, vcc
	v_add_f32_e32 v73, v73, v80
	v_cmp_eq_u32_e32 vcc, s76, v81
	s_waitcnt lgkmcnt(5)
	v_mov_b32_e32 v80, v89
	v_and_b32_e32 v81, -16, v247
	v_cndmask_b32_e32 v73, v242, v73, vcc
	v_add_f32_e32 v74, v74, v80
	v_cmp_eq_u32_e32 vcc, s76, v81
	s_waitcnt lgkmcnt(4)
	v_mov_b32_e32 v80, v90
	v_and_b32_e32 v81, -16, v248
	v_cndmask_b32_e32 v74, v242, v74, vcc
	v_add_f32_e32 v75, v75, v80
	v_cmp_eq_u32_e32 vcc, s76, v81
	s_waitcnt lgkmcnt(3)
	v_mov_b32_e32 v80, v91
	v_and_b32_e32 v81, -16, v249
	v_cndmask_b32_e32 v75, v242, v75, vcc
	v_add_f32_e32 v76, v76, v80
	v_cmp_eq_u32_e32 vcc, s76, v81
	s_waitcnt lgkmcnt(2)
	v_mov_b32_e32 v80, v92
	v_and_b32_e32 v81, -16, v250
	v_cndmask_b32_e32 v76, v242, v76, vcc
	v_add_f32_e32 v77, v77, v80
	v_cmp_eq_u32_e32 vcc, s76, v81
	s_waitcnt lgkmcnt(1)
	v_mov_b32_e32 v80, v251
	v_and_b32_e32 v81, -16, v239
	v_cndmask_b32_e32 v77, v242, v77, vcc
	v_add_f32_e32 v78, v78, v80
	v_cmp_eq_u32_e32 vcc, s76, v81
	s_waitcnt lgkmcnt(0)
	v_mov_b32_e32 v80, v94
	v_and_b32_e32 v81, -16, v93
	v_cndmask_b32_e32 v78, v242, v78, vcc
	v_add_f32_e32 v79, v79, v80
	v_cmp_eq_u32_e32 vcc, s76, v81
	v_mov_b64_e32 v[80:81], v[96:97]
	v_mov_b64_e32 v[82:83], v[98:99]
	v_cndmask_b32_e32 v79, v242, v79, vcc
	v_mov_b64_e32 v[84:85], v[100:101]
	v_mov_b64_e32 v[86:87], v[102:103]
	v_mov_b64_e32 v[88:89], v[104:105]
	v_mov_b64_e32 v[90:91], v[106:107]
	v_mov_b64_e32 v[92:93], v[108:109]
	v_mov_b64_e32 v[94:95], v[110:111]
	s_branch .LBB0_706

.LBB0_737:
	v_add_u32_e32 v0, s81, v226
	ds_read_b64_tr_b16 v[6:7], v0 offset:24576
	ds_read_b64_tr_b16 v[8:9], v0 offset:25088
	s_waitcnt lgkmcnt(9)
	v_mfma_f32_32x32x16_bf16 v[96:111], v[188:191], v[156:159], v[48:63]
	v_add_f32_e32 v2, v80, v81
	v_add_f32_e32 v2, v82, v2
	v_add_f32_e32 v2, v83, v2
	v_add_f32_e32 v2, v84, v2
	v_add_f32_e32 v10, v85, v2
	v_cvt_pk_bf16_f32 v140, v80, v81
	v_cvt_pk_bf16_f32 v141, v82, v83
	ds_read_b64_tr_b16 v[2:3], v0 offset:28672
	ds_read_b64_tr_b16 v[4:5], v0 offset:29184
	s_waitcnt lgkmcnt(10)
	v_mfma_f32_32x32x16_bf16 v[48:63], v[184:187], v[156:159], v[48:63]
	v_add_f32_e32 v10, v86, v10
	v_add_f32_e32 v10, v87, v10
	v_add_f32_e32 v10, v88, v10
	v_add_f32_e32 v14, v89, v10
	v_cvt_pk_bf16_f32 v142, v84, v85
	v_cvt_pk_bf16_f32 v143, v86, v87
	ds_read_b64_tr_b16 v[10:11], v0 offset:25600
	ds_read_b64_tr_b16 v[12:13], v0 offset:26112
	s_waitcnt lgkmcnt(11)
	v_mfma_f32_32x32x16_bf16 v[96:111], v[180:183], v[152:155], v[96:111]
	v_add_f32_e32 v14, v90, v14
	v_add_f32_e32 v14, v91, v14
	v_add_f32_e32 v14, v92, v14
	v_add_f32_e32 v14, v93, v14
	v_cvt_pk_bf16_f32 v136, v88, v89
	v_cvt_pk_bf16_f32 v137, v90, v91
	ds_read_b64_tr_b16 v[80:81], v0 offset:29696
	ds_read_b64_tr_b16 v[82:83], v0 offset:30208
	s_waitcnt lgkmcnt(12)
	v_mfma_f32_32x32x16_bf16 v[48:63], v[176:179], v[152:155], v[48:63]
	v_add_f32_e32 v14, v94, v14
	v_add_f32_e32 v14, v95, v14
	v_add_f32_e32 v14, v64, v14
	v_add_f32_e32 v14, v65, v14
	v_cvt_pk_bf16_f32 v138, v92, v93
	v_cvt_pk_bf16_f32 v139, v94, v95
	ds_read_b64_tr_b16 v[84:85], v0 offset:26624
	ds_read_b64_tr_b16 v[86:87], v0 offset:27136
	s_waitcnt lgkmcnt(13)
	v_mfma_f32_32x32x16_bf16 v[96:111], v[172:175], v[148:151], v[96:111]
	v_add_f32_e32 v14, v66, v14
	v_add_f32_e32 v14, v67, v14
	v_add_f32_e32 v14, v68, v14
	v_add_f32_e32 v14, v69, v14
	v_cvt_pk_bf16_f32 v132, v64, v65
	v_cvt_pk_bf16_f32 v133, v66, v67
	ds_read_b64_tr_b16 v[88:89], v0 offset:30720
	ds_read_b64_tr_b16 v[90:91], v0 offset:31232
	s_waitcnt lgkmcnt(14)
	v_mfma_f32_32x32x16_bf16 v[48:63], v[168:171], v[148:151], v[48:63]
	v_add_f32_e32 v14, v70, v14
	v_add_f32_e32 v14, v71, v14
	v_add_f32_e32 v14, v72, v14
	v_add_f32_e32 v14, v73, v14
	v_cvt_pk_bf16_f32 v134, v68, v69
	v_cvt_pk_bf16_f32 v135, v70, v71
	ds_read_b64_tr_b16 v[92:93], v0 offset:27648
	ds_read_b64_tr_b16 v[94:95], v0 offset:28160
	s_waitcnt lgkmcnt(14)
	v_mfma_f32_32x32x16_bf16 v[96:111], v[164:167], v[144:147], v[96:111]
	v_add_f32_e32 v14, v74, v14
	v_add_f32_e32 v14, v75, v14
	v_add_f32_e32 v14, v76, v14
	v_add_f32_e32 v14, v77, v14
	v_cvt_pk_bf16_f32 v128, v72, v73
	v_cvt_pk_bf16_f32 v129, v74, v75
	ds_read_b64_tr_b16 v[112:113], v0 offset:31744
	ds_read_b64_tr_b16 v[114:115], v0 offset:32256
	v_mfma_f32_32x32x16_bf16 v[48:63], v[160:163], v[144:147], v[48:63]
	v_add_f32_e32 v0, v78, v14
	v_add_f32_e32 v0, v79, v0
	v_add_f32_e32 v0, 0, v0
	v_cvt_pk_bf16_f32 v130, v76, v77
	v_cvt_pk_bf16_f32 v131, v78, v79
	s_cmp_lt_i32 s0, 5
	s_cbranch_scc1 .LBB0_771
	s_add_i32 s65, s65, s63
	s_max_i32 s0, s65, 4
	s_add_i32 s0, s0, -4
	s_min_u32 s0, s0, 56
	s_add_i32 s13, s13, s12
	s_sub_i32 s0, s13, s0
	s_cmp_gt_u32 s0, 7
	s_cselect_b64 vcc, -1, 0
	s_cbranch_scc1 .Lna_allmask_4
	s_sub_i32 s0, s13, s65
	s_max_i32 s0, s0, -7
	s_add_i32 s0, s0, 7
	s_min_u32 s0, s0, 14
	s_mulk_i32 s0, 0x7c
	v_lshlrev_b32_e32 v14, 2, v224
	v_add3_u32 v116, v225, s0, v14
	ds_read_b32 v15, v116 offset:128
	ds_read_b32 v64, v116
	ds_read_b32 v65, v116 offset:4
	ds_read_b32 v66, v116 offset:8
	ds_read_b32 v67, v116 offset:12
	ds_read_b32 v68, v116 offset:32
	ds_read_b32 v69, v116 offset:36
	v_cmp_gt_u32_e32 vcc, 16, v223
	s_waitcnt lgkmcnt(5)
	v_add_f32_e32 v64, v96, v64
	v_cndmask_b32_e32 v64, v242, v64, vcc
	ds_read_b32 v70, v116 offset:40
	ds_read_b32 v96, v116 offset:132
	v_add_u32_e32 v117, 1, v223
	v_cmp_gt_u32_e32 vcc, 16, v117
	s_waitcnt lgkmcnt(6)
	v_add_f32_e32 v65, v97, v65
	v_cndmask_b32_e32 v65, v242, v65, vcc
	ds_read_b32 v71, v116 offset:44
	ds_read_b32 v97, v116 offset:136
	v_add_u32_e32 v118, 2, v223
	v_cmp_gt_u32_e32 vcc, 16, v118
	s_waitcnt lgkmcnt(7)
	v_add_f32_e32 v66, v98, v66
	v_cndmask_b32_e32 v66, v242, v66, vcc
	ds_read_b32 v72, v116 offset:64
	ds_read_b32 v98, v116 offset:140
	v_add_u32_e32 v119, 3, v223
	v_cmp_gt_u32_e32 vcc, 16, v119
	s_waitcnt lgkmcnt(8)
	v_add_f32_e32 v67, v99, v67
	v_cndmask_b32_e32 v67, v242, v67, vcc
	ds_read_b32 v73, v116 offset:68
	ds_read_b32 v99, v116 offset:160
	v_add_u32_e32 v120, 8, v223
	v_cmp_gt_u32_e32 vcc, 16, v120
	s_waitcnt lgkmcnt(9)
	v_add_f32_e32 v68, v100, v68
	v_cndmask_b32_e32 v68, v242, v68, vcc
	ds_read_b32 v74, v116 offset:72
	ds_read_b32 v100, v116 offset:164
	v_add_u32_e32 v121, 9, v223
	v_cmp_gt_u32_e32 vcc, 16, v121
	s_waitcnt lgkmcnt(10)
	v_add_f32_e32 v69, v101, v69
	v_cndmask_b32_e32 v69, v242, v69, vcc
	ds_read_b32 v75, v116 offset:76
	ds_read_b32 v101, v116 offset:168
	v_add_u32_e32 v122, 10, v223
	v_cmp_gt_u32_e32 vcc, 16, v122
	s_waitcnt lgkmcnt(11)
	v_add_f32_e32 v70, v102, v70
	v_cndmask_b32_e32 v70, v242, v70, vcc
	ds_read_b32 v76, v116 offset:96
	ds_read_b32 v102, v116 offset:172
	v_add_u32_e32 v123, 11, v223
	v_cmp_gt_u32_e32 vcc, 16, v123
	s_waitcnt lgkmcnt(11)
	v_add_f32_e32 v71, v103, v71
	v_cndmask_b32_e32 v71, v242, v71, vcc
	ds_read_b32 v77, v116 offset:100
	ds_read_b32 v103, v116 offset:192
	v_cmp_lt_u32_e32 vcc, s79, v223
	s_waitcnt lgkmcnt(11)
	v_add_f32_e32 v72, v104, v72
	v_cndmask_b32_e32 v72, v242, v72, vcc
	ds_read_b32 v78, v116 offset:104
	ds_read_b32 v104, v116 offset:196
	v_add_u32_e32 v124, 17, v223
	v_cmp_gt_u32_e32 vcc, 16, v124
	s_waitcnt lgkmcnt(11)
	v_add_f32_e32 v73, v105, v73
	v_cndmask_b32_e32 v73, v242, v73, vcc
	ds_read_b32 v79, v116 offset:108
	ds_read_b32 v105, v116 offset:200
	v_add_u32_e32 v125, 18, v223
	v_cmp_gt_u32_e32 vcc, 16, v125
	s_waitcnt lgkmcnt(11)
	v_add_f32_e32 v74, v106, v74
	v_cndmask_b32_e32 v74, v242, v74, vcc
	ds_read_b32 v106, v116 offset:204
	v_add_u32_e32 v126, 19, v223
	v_cmp_gt_u32_e32 vcc, 16, v126
	s_waitcnt lgkmcnt(10)
	v_add_f32_e32 v75, v107, v75
	v_cndmask_b32_e32 v75, v242, v75, vcc
	ds_read_b32 v107, v116 offset:224
	v_add_u32_e32 v127, 24, v223
	v_cmp_gt_u32_e32 vcc, 16, v127
	s_waitcnt lgkmcnt(9)
	v_add_f32_e32 v76, v108, v76
	v_cndmask_b32_e32 v76, v242, v76, vcc
	ds_read_b32 v108, v116 offset:228
	v_add_u32_e32 v144, 25, v223
	v_cmp_gt_u32_e32 vcc, 16, v144
	s_waitcnt lgkmcnt(8)
	v_add_f32_e32 v77, v109, v77
	v_cndmask_b32_e32 v77, v242, v77, vcc
	ds_read_b32 v145, v116 offset:232
	v_add_u32_e32 v146, 26, v223
	v_cmp_gt_u32_e32 vcc, 16, v146
	s_waitcnt lgkmcnt(7)
	v_add_f32_e32 v78, v110, v78
	v_cndmask_b32_e32 v78, v242, v78, vcc
	ds_read_b32 v110, v116 offset:236
	v_add_u32_e32 v109, 27, v223
	v_cmp_gt_u32_e32 vcc, 16, v109
	s_waitcnt lgkmcnt(6)
	v_add_f32_e32 v79, v111, v79
	v_cndmask_b32_e32 v79, v242, v79, vcc
	s_waitcnt lgkmcnt(14)
	v_and_b32_e32 v111, -16, v223
	v_add_f32_e32 v15, v48, v15
	v_cmp_eq_u32_e32 vcc, s76, v111
	s_nop 1
	v_cndmask_b32_e32 v48, v242, v15, vcc
	v_mov_b32_e32 v15, v96
	v_and_b32_e32 v96, -16, v117
	v_add_f32_e32 v15, v49, v15
	v_cmp_eq_u32_e32 vcc, s76, v96
	v_and_b32_e32 v96, -16, v118
	s_nop 0
	v_cndmask_b32_e32 v49, v242, v15, vcc
	s_waitcnt lgkmcnt(13)
	v_mov_b32_e32 v15, v97
	v_add_f32_e32 v15, v50, v15
	v_cmp_eq_u32_e32 vcc, s76, v96
	v_and_b32_e32 v96, -16, v119
	s_nop 0
	v_cndmask_b32_e32 v50, v242, v15, vcc
	s_waitcnt lgkmcnt(12)
	v_mov_b32_e32 v15, v98
	v_add_f32_e32 v15, v51, v15
	v_cmp_eq_u32_e32 vcc, s76, v96
	v_and_b32_e32 v96, -16, v120
	s_nop 0
	v_cndmask_b32_e32 v51, v242, v15, vcc
	s_waitcnt lgkmcnt(11)
	v_mov_b32_e32 v15, v99
	v_add_f32_e32 v15, v52, v15
	v_cmp_eq_u32_e32 vcc, s76, v96
	v_and_b32_e32 v96, -16, v121
	s_nop 0
	v_cndmask_b32_e32 v52, v242, v15, vcc
	s_waitcnt lgkmcnt(10)
	v_mov_b32_e32 v15, v100
	v_add_f32_e32 v15, v53, v15
	v_cmp_eq_u32_e32 vcc, s76, v96
	v_and_b32_e32 v96, -16, v122
	s_nop 0
	v_cndmask_b32_e32 v53, v242, v15, vcc
	s_waitcnt lgkmcnt(9)
	v_mov_b32_e32 v15, v101
	v_add_f32_e32 v15, v54, v15
	v_cmp_eq_u32_e32 vcc, s76, v96
	v_and_b32_e32 v96, -16, v123
	s_nop 0
	v_cndmask_b32_e32 v54, v242, v15, vcc
	s_waitcnt lgkmcnt(8)
	v_mov_b32_e32 v15, v102
	v_add_f32_e32 v15, v55, v15
	v_cmp_eq_u32_e32 vcc, s76, v96
	v_and_b32_e32 v96, -16, v124
	s_nop 0
	v_cndmask_b32_e32 v55, v242, v15, vcc
	s_waitcnt lgkmcnt(7)
	v_mov_b32_e32 v15, v103
	v_add_f32_e32 v15, v56, v15
	v_cmp_eq_u32_e32 vcc, s78, v111
	s_nop 1
	v_cndmask_b32_e32 v56, v242, v15, vcc
	s_waitcnt lgkmcnt(6)
	v_mov_b32_e32 v15, v104
	v_add_f32_e32 v15, v57, v15
	v_cmp_eq_u32_e32 vcc, s76, v96
	v_and_b32_e32 v96, -16, v125
	s_nop 0
	v_cndmask_b32_e32 v57, v242, v15, vcc
	s_waitcnt lgkmcnt(5)
	v_mov_b32_e32 v15, v105
	v_add_f32_e32 v15, v58, v15
	v_cmp_eq_u32_e32 vcc, s76, v96
	v_and_b32_e32 v96, -16, v126
	s_nop 0
	v_cndmask_b32_e32 v58, v242, v15, vcc
	s_waitcnt lgkmcnt(4)
	v_mov_b32_e32 v15, v106
	v_add_f32_e32 v15, v59, v15
	v_cmp_eq_u32_e32 vcc, s76, v96
	v_and_b32_e32 v96, -16, v127
	s_nop 0
	v_cndmask_b32_e32 v59, v242, v15, vcc
	s_waitcnt lgkmcnt(3)
	v_mov_b32_e32 v15, v107
	v_add_f32_e32 v15, v60, v15
	v_cmp_eq_u32_e32 vcc, s76, v96
	v_and_b32_e32 v96, -16, v144
	s_nop 0
	v_cndmask_b32_e32 v60, v242, v15, vcc
	s_waitcnt lgkmcnt(2)
	v_mov_b32_e32 v15, v108
	v_add_f32_e32 v15, v61, v15
	v_cmp_eq_u32_e32 vcc, s76, v96
	v_and_b32_e32 v96, -16, v146
	s_nop 0
	v_cndmask_b32_e32 v61, v242, v15, vcc
	s_waitcnt lgkmcnt(1)
	v_mov_b32_e32 v15, v145
	v_add_f32_e32 v15, v62, v15
	v_cmp_eq_u32_e32 vcc, s76, v96
	s_waitcnt lgkmcnt(0)
	v_mov_b32_e32 v14, v110
	v_add_f32_e32 v14, v63, v14
	v_cndmask_b32_e32 v62, v242, v15, vcc
	v_and_b32_e32 v15, -16, v109
	v_cmp_eq_u32_e32 vcc, s76, v15
	v_mov_b64_e32 v[110:111], v[78:79]
	v_mov_b64_e32 v[108:109], v[76:77]
	v_cndmask_b32_e32 v63, v242, v14, vcc
	v_mov_b64_e32 v[106:107], v[74:75]
	v_mov_b64_e32 v[104:105], v[72:73]
	v_mov_b64_e32 v[102:103], v[70:71]
	v_mov_b64_e32 v[100:101], v[68:69]
	v_mov_b64_e32 v[98:99], v[66:67]
	v_mov_b64_e32 v[96:97], v[64:65]
	s_branch .LBB0_771
.Lna_allmask_4:
	v_mov_b32_e32 v96, v242
	v_mov_b32_e32 v97, v242
	v_mov_b32_e32 v98, v242
	v_mov_b32_e32 v99, v242
	v_mov_b32_e32 v100, v242
	v_mov_b32_e32 v101, v242
	v_mov_b32_e32 v102, v242
	v_mov_b32_e32 v103, v242
	v_mov_b32_e32 v104, v242
	v_mov_b32_e32 v105, v242
	v_mov_b32_e32 v106, v242
	v_mov_b32_e32 v107, v242
	v_mov_b32_e32 v108, v242
	v_mov_b32_e32 v109, v242
	v_mov_b32_e32 v110, v242
	v_mov_b32_e32 v111, v242
	v_mov_b32_e32 v48, v242
	v_mov_b32_e32 v49, v242
	v_mov_b32_e32 v50, v242
	v_mov_b32_e32 v51, v242
	v_mov_b32_e32 v52, v242
	v_mov_b32_e32 v53, v242
	v_mov_b32_e32 v54, v242
	v_mov_b32_e32 v55, v242
	v_mov_b32_e32 v56, v242
	v_mov_b32_e32 v57, v242
	v_mov_b32_e32 v58, v242
	v_mov_b32_e32 v59, v242
	v_mov_b32_e32 v60, v242
	v_mov_b32_e32 v61, v242
	v_mov_b32_e32 v62, v242
	v_mov_b32_e32 v63, v242
